# phases B and D: odd workgroups run their weight-conversion share first and the token/attention work second (even workgroups keep the order), so conversion and compute of different workgroups overlap
# speedup vs baseline: 1.0166x; 1.0073x over previous
; __global__ void __launch_bounds__(512, 2) mega(Args a) {
;     ...
; #pragma unroll 1
;     for (int l = 0; l < NLAYER; ++l) {
;         const int pb = 2 + 10 * l;
.LBB0_127:
	s_waitcnt lgkmcnt(0)
	s_barrier
	s_mov_b32 s0, 0
	v_writelane_b32 v255, s0, 44
	v_writelane_b32 v255, s0, 45
	s_nop 1

; #define LAS __attribute__((address_space(3)))
; __global__ void __launch_bounds__(512, 2) mega(Args a) {
;     ...
;             if (l + 1 < NLAYER && vcu >= 8) {
;                 LAS float* scr = (LAS float*)(lds + wave * 16384);
;                 for (int it = (vcu - 8) * 8 + wave; it < IT_LAYER / 2; it += (G - 8) * 8) CONVERT_ITEM(l + 1, it);
.Lb_reenter:
	v_readlane_b32 s0, v254, 52
	s_lshl_b32 s62, s0, 8
	s_lshl_b32 s23, s0, 2
	s_cmp_eq_u32 s0, 3
	s_cselect_b64 s[2:3], -1, 0
	v_readlane_b32 s1, v254, 53
	v_writelane_b32 v254, s2, 56
	s_cmp_lg_u32 s0, 3
	v_readlane_b32 s40, v253, 58
	v_writelane_b32 v254, s3, 57
	s_cselect_b64 s[2:3], -1, 0
	s_add_i32 s16, s0, 1
	v_readlane_b32 s0, v253, 32
	v_readlane_b32 s1, v253, 33
	s_mov_b32 s5, s1
	s_lshl_b32 s4, s16, 20
	s_lshl_b32 s21, s16, 5
	s_lshl_b64 s[0:1], s[4:5], 2
	v_writelane_b32 v254, s2, 58
	v_readlane_b32 s41, v253, 59
	s_add_u32 s0, s40, s0
	v_writelane_b32 v254, s3, 59
	s_addc_u32 s1, s41, s1
	v_readlane_b32 s46, v254, 0
	v_readlane_b32 s47, v254, 1
	v_readlane_b32 s48, v254, 2
	v_readlane_b32 s49, v254, 3
	v_readlane_b32 s50, v254, 4
	v_readlane_b32 s51, v254, 5
	v_readlane_b32 s52, v254, 6
	v_readlane_b32 s53, v254, 7
	v_readlane_b32 s54, v254, 8
	v_readlane_b32 s55, v254, 9
	v_writelane_b32 v254, s0, 60
	v_readlane_b32 s2, v246, 13
	v_readlane_b32 s3, v246, 14
	v_writelane_b32 v254, s1, 61
	s_lshl_b32 s0, s16, 21
	s_add_u32 s0, s2, s0
	s_addc_u32 s1, s3, 0
	v_writelane_b32 v254, s0, 62
	v_readlane_b32 s42, v253, 60
	v_readlane_b32 s43, v253, 61
	v_writelane_b32 v254, s1, 63
	s_mov_b32 s1, s5
	v_readlane_b32 s44, v253, 62
	v_readlane_b32 s45, v253, 63
	v_writelane_b32 v253, s0, 32
	s_mov_b32 s17, s5
	v_readlane_b32 s2, v246, 11
	v_writelane_b32 v253, s1, 33
	s_lshl_b64 s[0:1], s[16:17], 20
	v_readlane_b32 s8, v253, 38
	v_readlane_b32 s9, v253, 39
	s_add_u32 s0, s8, s0
	s_addc_u32 s1, s9, s1
	v_writelane_b32 v255, s0, 0
	v_readlane_b32 s3, v246, 12
	v_readlane_b32 s10, v253, 40
	v_writelane_b32 v255, s1, 1
	s_lshl_b64 s[0:1], s[16:17], 19
	s_add_u32 s0, s2, s0
	v_readlane_b32 s11, v253, 41
	s_addc_u32 s1, s3, s1
	v_writelane_b32 v255, s0, 2
	v_readlane_b32 s8, v253, 42
	v_readlane_b32 s14, v253, 48
	v_writelane_b32 v255, s1, 3
	s_mul_i32 s1, s16, 0x120000
	s_mul_hi_u32 s0, s16, 0x120000
	v_readlane_b32 s15, v253, 49
	s_add_u32 s2, s14, s1
	s_addc_u32 s3, s15, s0
	v_writelane_b32 v255, s2, 4
	s_mul_i32 s1, s16, 0x90000
	s_mul_hi_u32 s0, s16, 0x90000
	v_writelane_b32 v255, s3, 5
	v_readlane_b32 s2, v246, 9
	v_readlane_b32 s3, v246, 10
	s_add_u32 s2, s2, s1
	s_addc_u32 s3, s3, s0
	v_writelane_b32 v255, s2, 6
	s_mul_i32 s1, s16, 0x7c0000
	v_readlane_b32 s9, v253, 43
	v_writelane_b32 v255, s3, 7
	s_mul_hi_u32 s0, s16, 0x7c0000
	s_add_u32 s2, s8, s1
	s_addc_u32 s3, s9, s0
	v_writelane_b32 v255, s2, 8
	s_mov_b32 s0, s16
	v_readlane_b32 s10, v253, 44
	v_writelane_b32 v255, s3, 9
	v_writelane_b32 v255, s0, 10
	v_readlane_b32 s2, v246, 7
	v_readlane_b32 s3, v246, 8
	v_writelane_b32 v255, s1, 11
	s_lshl_b64 s[0:1], s[16:17], 21
	s_add_u32 s0, s2, s0
	s_addc_u32 s1, s3, s1
	v_writelane_b32 v255, s0, 12
	s_andn2_b64 vcc, exec, s[6:7]
	v_readlane_b32 s11, v253, 45
	v_writelane_b32 v255, s1, 13
	v_readlane_b32 s0, v247, 63
	v_readlane_b32 s1, v248, 0
	v_readlane_b32 s12, v253, 46
	v_readlane_b32 s13, v253, 47
	s_waitcnt vmcnt(0)
	v_cndmask_b32_e64 v0, 0, 1, s[0:1]
	v_cmp_ne_u32_e64 s[84:85], 1, v0
	s_cbranch_vccnz .LBB0_364
	v_mbcnt_lo_u32_b32 v100, -1, 0
	v_mbcnt_hi_u32_b32 v100, -1, v100
	s_and_b64 vcc, exec, s[84:85]
	s_nop 0
	v_and_b32_e32 v97, 31, v100
	v_ashrrev_i32_e32 v96, 5, v100
	v_lshlrev_b32_e32 v98, 2, v97
	s_cbranch_vccnz .LBB0_328
	v_readlane_b32 s0, v255, 44
	s_nop 3
	s_cmp_lg_u32 s0, 0
	s_cbranch_scc1 .Lb_chunk
	v_readlane_b32 s0, v246, 4
	s_nop 3
	s_bitcmp1_b32 s0, 0
	s_cbranch_scc0 .Lb_chunk
	v_readlane_b32 s0, v248, 13
	s_nop 3
	s_cmp_lg_u32 s0, 0
	s_cbranch_scc1 .Lb_chunk
	v_readlane_b32 s0, v254, 56
	s_nop 3
	s_cmp_lg_u32 s0, 0
	s_cbranch_scc1 .Lb_chunk
	v_readlane_b32 s0, v248, 16
	s_nop 3
	s_cmp_lg_u32 s0, 0
	s_cbranch_scc1 .Lb_chunk
	s_mov_b32 s0, 2
	v_writelane_b32 v255, s0, 44
	s_nop 1
	s_branch .LBB0_328
; #define LAS __attribute__((address_space(3)))
; __global__ void __launch_bounds__(512, 2) mega(Args a) {
;     ...
;             const float* qg = a.in[I_QNG] + l * 384; const float* kvg = a.in[I_KVNG] + l * 256;
;             const float* sgg = a.in[I_SGNG] + l * 256; const float* sgb = a.in[I_SGNB] + l * 256;
;             const float* sb = a.in[I_SGB] + l * 4 * 128;
;             LAS float* ksr = (LAS float*)lds;
;             LAS bf16_t* vsT = (LAS bf16_t*)(lds + 65536);
;             constexpr int VST = 136;
;             for (int T = vcu; T < NTOK / 128; T += G) {
;                 const int n0 = T * 128;
;                 float qgv[6];
; #pragma unroll
;                 for (int j = 0; j < 3; ++j) { qgv[2 * j] = qg[lane * 2 + 128 * j]; qgv[2 * j + 1] = qg[lane * 2 + 128 * j + 1]; }
;                 const f32x4 kvgv = *(const f32x4*)(kvg + lane * 4), sggv = *(const f32x4*)(sgg + lane * 4), sgbv = *(const f32x4*)(sgb + lane * 4);
.Lb_chunk:
	v_readlane_b32 s16, v253, 32
	v_readlane_b32 s4, v254, 52
	v_readlane_b32 s17, v253, 33
	s_mul_i32 s16, s4, 0x180
	v_readlane_b32 s8, v253, 42
	s_lshl_b64 s[0:1], s[16:17], 2
	v_readlane_b32 s10, v253, 44
	v_readlane_b32 s9, v253, 43
	v_readlane_b32 s11, v253, 45
	s_add_u32 s0, s10, s0
	s_mov_b32 s63, s17
	v_readlane_b32 s12, v253, 46
	s_addc_u32 s1, s11, s1
	s_lshl_b64 s[8:9], s[62:63], 2
	v_readlane_b32 s13, v253, 47
	v_readlane_b32 s14, v253, 48
	v_readlane_b32 s15, v253, 49
	s_add_u32 s10, s12, s8
	s_addc_u32 s11, s13, s9
	v_readlane_b32 s12, v253, 38
	v_readlane_b32 s14, v253, 40
	v_readlane_b32 s13, v253, 39
	v_readlane_b32 s15, v253, 41
	s_add_u32 s12, s14, s8
	s_addc_u32 s13, s15, s9
	v_readlane_b32 s2, v253, 36
	v_readlane_b32 s3, v253, 37
	s_add_u32 s14, s2, s8
	s_addc_u32 s15, s3, s9
	s_lshl_b32 s16, s4, 9
	v_lshlrev_b32_e32 v2, 2, v100
	s_lshl_b64 s[8:9], s[16:17], 2
	v_readlane_b32 s2, v253, 24
	v_ashrrev_i32_e32 v3, 31, v2
	v_readlane_b32 s3, v253, 25
	s_add_u32 s8, s2, s8
	v_lshlrev_b64 v[4:5], 2, v[2:3]
	v_and_b32_e32 v160, 15, v100
	v_ashrrev_i32_e32 v7, 4, v100
	s_addc_u32 s9, s3, s9
	v_readlane_b32 s2, v248, 7
	v_lshl_add_u64 v[102:103], s[10:11], 0, v[4:5]
	v_lshl_add_u64 v[104:105], s[12:13], 0, v[4:5]
	v_lshl_add_u64 v[106:107], s[14:15], 0, v[4:5]
	v_lshl_add_u64 v[108:109], v[2:3], 1, s[92:93]
	v_and_b32_e32 v2, 1, v7
	v_lshlrev_b32_e32 v3, 1, v160
	v_and_b32_e32 v4, 0xffffffe0, v100
	v_readlane_b32 s3, v248, 8
	v_cmp_eq_u32_e64 s[44:45], 0, v2
	v_or3_b32 v2, v4, v3, v2
	s_add_i32 s16, s23, s2
	v_add_u32_e32 v2, 0x80, v2
	v_readlane_b32 s2, v246, 29
	v_ashrrev_i32_e32 v3, 31, v2
	v_readlane_b32 s3, v246, 30
	v_readlane_b32 s5, v254, 53
	v_readlane_b32 s4, v246, 35
	v_lshl_add_u64 v[110:111], s[2:3], 0, v[2:3]
	s_movk_i32 s2, 0x440
	v_mul_lo_u32 v2, v100, s2
	s_add_i32 s2, 0, 0x10000
	v_add_u32_e32 v161, s2, v2
	v_lshlrev_b32_e32 v2, 5, v7
	v_ashrrev_i32_e32 v3, 31, v2
	v_lshlrev_b64 v[2:3], 2, v[2:3]
	v_readlane_b32 s5, v246, 36
	v_lshlrev_b32_e32 v0, 1, v100
	v_readlane_b32 s3, v248, 6
	v_lshl_add_u64 v[4:5], s[4:5], 0, v[2:3]
	v_readlane_b32 s4, v246, 37
	v_readlane_b32 s5, v246, 38
	v_ashrrev_i32_e32 v1, 31, v0
	v_lshlrev_b32_e32 v152, 2, v160
	v_lshl_add_u64 v[2:3], s[4:5], 0, v[2:3]
	v_add_u32_e32 v173, s3, v98
	v_readlane_b32 s3, v248, 5
	v_lshl_add_u64 v[114:115], v[2:3], 0, v[152:153]
	v_lshlrev_b32_e32 v2, 7, v7
	v_lshl_or_b32 v7, v97, 1, s3
	v_lshl_add_u64 v[118:119], v[0:1], 2, s[0:1]
	s_movk_i32 s0, 0x110
	v_mul_lo_u32 v10, v7, s0
	v_mad_i64_i32 v[122:123], s[0:1], v100, -6, 0
	v_readlane_b32 s0, v251, 0
	v_readlane_b32 s1, v251, 1
	v_readlane_b32 s4, v248, 11
	v_mov_b32_e32 v99, v153
	v_lshl_add_u64 v[124:125], v[0:1], 1, s[0:1]
	v_readlane_b32 s0, v250, 61
	v_readlane_b32 s1, v250, 62
	v_lshl_add_u64 v[112:113], v[4:5], 0, v[152:153]
	v_add3_u32 v172, 0, v2, v152
	v_lshlrev_b32_e32 v152, 3, v97
	v_readlane_b32 s5, v248, 12
	v_lshl_add_u64 v[126:127], s[0:1], 0, v[98:99]
	v_readlane_b32 s0, v248, 53
	v_lshl_add_u64 v[116:117], s[4:5], 0, v[152:153]
	v_lshlrev_b32_e32 v152, 1, v7
	v_readlane_b32 s1, v248, 54
	v_lshlrev_b32_e32 v9, 2, v96
	v_ashrrev_i32_e32 v101, 31, v100
	v_lshl_add_u64 v[130:131], s[0:1], 0, v[152:153]
	v_readlane_b32 s0, v251, 59
	v_lshlrev_b32_e32 v2, 3, v96
	v_lshlrev_b64 v[120:121], 2, v[100:101]
	v_add_u32_e32 v99, s0, v9
	v_readlane_b32 s0, v251, 61
	v_ashrrev_i32_e32 v3, 31, v2
	v_lshl_add_u64 v[128:129], s[26:27], 0, v[152:153]
	v_add_u32_e32 v101, s0, v9
	v_readlane_b32 s0, v251, 60
	v_and_b32_e32 v6, 0xffffffe0, v0
	v_lshl_add_u32 v8, v96, 4, s2
	v_add_lshl_u32 v152, s0, v97, 8
	v_readlane_b32 s0, v251, 63
	v_lshl_add_u64 v[2:3], v[2:3], 1, v[152:153]
	v_readlane_b32 s1, v252, 0
	v_ashrrev_i32_e32 v5, 31, v6
	v_or_b32_e32 v4, v6, v160
	v_lshl_add_u64 v[132:133], s[0:1], 0, v[2:3]
	s_mov_b32 s1, s17
	v_writelane_b32 v253, s0, 32
	v_cmp_gt_u32_e64 s[42:43], 32, v100
	v_lshlrev_b64 v[134:135], 1, v[0:1]
	v_lshlrev_b64 v[136:137], 1, v[4:5]
	v_writelane_b32 v253, s1, 33
	s_lshl_b64 s[10:11], s[16:17], 2
	v_add_u32_e32 v152, v8, v10
	v_readlane_b32 s5, v246, 4
	s_branch .LBB0_267

; #define LAS __attribute__((address_space(3)))
; __device__ __forceinline__ unsigned pk4_fp8(float x0, float x1, float x2, float x3) { int w = 0; w = __builtin_amdgcn_cvt_pk_fp8_f32(x0, x1, w, false); w = __builtin_amdgcn_cvt_pk_fp8_f32(x2, x3, w, true); return (unsigned)w; }
; __device__ __forceinline__ void transpose_item_fp8w(const float* W, int K, int N, unsigned char* WT, float q, LAS unsigned char* scr, int item, int lane) {
;     const int nblk = N / 128, kb = item / nblk, nb = item % nblk, k0 = 64 * kb, n0 = 128 * nb;
;     const int l5 = lane & 31, h = lane >> 5;
;     const float* src = W + (size_t)(k0 + 16 * h) * N + n0 + 4 * l5;
; #pragma unroll
;     for (int b = 0; b < 2; ++b) {
;         f32x4 x[16];
; #pragma unroll
;         for (int s_ = 0; s_ < 16; ++s_) x[s_] = *(const f32x4*)(src + (size_t)(32 * b + s_) * N);
; #pragma unroll
;         for (int i = 0; i < 4; ++i) {
;             u32x4 o;
;             o.x = pk4_fp8(x[0][i] * q, x[1][i] * q, x[2][i] * q, x[3][i] * q); o.y = pk4_fp8(x[4][i] * q, x[5][i] * q, x[6][i] * q, x[7][i] * q);
;             o.z = pk4_fp8(x[8][i] * q, x[9][i] * q, x[10][i] * q, x[11][i] * q); o.w = pk4_fp8(x[12][i] * q, x[13][i] * q, x[14][i] * q, x[15][i] * q);
;             *(LAS u32x4*)(scr + (l5 + 32 * i) * 80 + (2 * b + h) * 16) = o; }
;     }
;     asm volatile("s_waitcnt lgkmcnt(0)" ::: "memory");
; #pragma unroll
;     for (int qd = 0; qd < 8; ++qd) {
;         const int rho = 16 * qd + (lane >> 2), piece = lane & 3;
; __global__ void __launch_bounds__(512, 2) mega(Args a) {
;     ...
;             __syncthreads();
;             if (l + 1 < NLAYER && vcu >= 8) {
;                 LAS float* scr = (LAS float*)(lds + wave * 16384);
;                 for (int it = (vcu - 8) * 8 + wave; it < IT_LAYER / 2; it += (G - 8) * 8) CONVERT_ITEM(l + 1, it);
;             }
.LBB0_328:
	v_readlane_b32 s0, v255, 44
	s_nop 3
	s_cmp_eq_u32 s0, 1
	s_cbranch_scc1 .Lb_skipconv
	v_readlane_b32 s0, v248, 13
	v_readlane_b32 s2, v254, 56
	v_readlane_b32 s1, v248, 14
	v_readlane_b32 s3, v254, 57
	s_or_b64 s[0:1], s[2:3], s[0:1]
	v_readlane_b32 s2, v248, 16
	v_readlane_b32 s3, v248, 17
	s_or_b64 s[0:1], s[0:1], s[2:3]
	s_andn2_b64 vcc, exec, s[0:1]
	s_waitcnt vmcnt(0)
	s_barrier
	s_cbranch_vccz .LBB0_363
	v_ashrrev_i32_e32 v0, 1, v100
	v_lshlrev_b32_e32 v1, 4, v100
	v_and_b32_e32 v101, -16, v0
	v_ashrrev_i32_e32 v0, 2, v100
	v_and_b32_e32 v64, 48, v1
	v_and_b32_e32 v1, 0x7c, v100
	v_ashrrev_i32_e32 v6, 7, v100
	v_add_u32_e32 v102, v1, v6
	v_add_u32_e32 v6, 16, v0
	v_lshlrev_b32_e32 v7, 2, v6
	v_and_b32_e32 v7, 0x7c, v7
	v_ashrrev_i32_e32 v6, 5, v6
	v_add_u32_e32 v103, v7, v6
	v_add_u32_e32 v6, 32, v0
	v_ashrrev_i32_e32 v6, 5, v6
	v_add_u32_e32 v104, v1, v6
	v_add_u32_e32 v6, 48, v0
	v_lshlrev_b32_e32 v7, 2, v6
	v_and_b32_e32 v7, 0x7c, v7
	v_ashrrev_i32_e32 v6, 5, v6
	v_add_u32_e32 v105, v7, v6
	v_add_u32_e32 v6, 64, v0
	v_ashrrev_i32_e32 v6, 5, v6
	v_add_u32_e32 v106, v1, v6
	v_add_u32_e32 v6, 0x50, v0
	v_lshlrev_b32_e32 v7, 2, v6
	v_and_b32_e32 v7, 0x7c, v7
	v_ashrrev_i32_e32 v6, 5, v6
	s_movk_i32 s1, 0x50
	v_add_u32_e32 v107, v7, v6
	v_add_u32_e32 v6, 0x60, v0
	v_mul_lo_u32 v5, v0, s1
	v_ashrrev_i32_e32 v6, 5, v6
	v_add_u32_e32 v0, 0x70, v0
	v_add_u32_e32 v108, v1, v6
	v_lshlrev_b32_e32 v1, 2, v0
	v_and_b32_e32 v1, 0x7c, v1
	v_ashrrev_i32_e32 v0, 5, v0
	v_add_u32_e32 v109, v1, v0
	v_lshlrev_b32_e32 v0, 3, v100
	v_ashrrev_i32_e32 v110, 3, v100
	v_and_b32_e32 v152, 56, v0
	v_readlane_b32 s0, v246, 21
	v_mul_u32_u24_e32 v6, 0x84, v152
	v_lshlrev_b32_e32 v7, 2, v110
	v_add_u32_e32 v2, s0, v101
	v_add_u32_e32 v4, s0, v64
	v_add_u32_e32 v68, s0, v98
	v_add3_u32 v111, s0, v6, v7
	v_readlane_b32 s0, v255, 0
	v_mov_b32_e32 v99, v153
	v_readlane_b32 s1, v255, 1
	v_lshlrev_b32_e32 v0, 1, v152
	v_mov_b32_e32 v1, v153
	v_lshl_add_u64 v[72:73], s[0:1], 0, v[98:99]
	v_readlane_b32 s0, v255, 2
	v_readlane_b32 s1, v255, 3
	v_readlane_b32 s2, v254, 60
	v_readlane_b32 s3, v254, 61
	v_lshl_add_u64 v[74:75], s[0:1], 0, v[0:1]
	v_readlane_b32 s0, v255, 4
	v_readlane_b32 s1, v255, 5
	v_lshl_add_u64 v[66:67], s[2:3], 0, v[98:99]
	v_readlane_b32 s2, v254, 62
	v_lshl_add_u64 v[76:77], s[0:1], 0, v[98:99]
	v_readlane_b32 s0, v255, 6
	v_readlane_b32 s1, v255, 7
	v_mul_u32_u24_e32 v3, 0x50, v97
	v_readlane_b32 s3, v254, 63
	v_lshl_add_u64 v[78:79], s[0:1], 0, v[0:1]
	v_readlane_b32 s0, v255, 8
	v_readlane_b32 s1, v255, 9
	v_add_u32_e32 v84, 4, v96
	v_add_u32_e32 v86, 8, v96
	v_lshl_add_u64 v[80:81], s[0:1], 0, v[98:99]
	v_readlane_b32 s0, v255, 12
	v_readlane_b32 s1, v255, 13
	v_add_u32_e32 v88, 12, v96
	v_add_u32_e32 v90, 16, v96
	v_add_u32_e32 v92, 20, v96
	v_add_u32_e32 v94, 24, v96
	v_add_u32_e32 v100, 28, v96
	v_mov_b32_e32 v65, v153
	v_lshl_add_u64 v[70:71], s[2:3], 0, v[0:1]
	v_add_u32_e32 v112, 8, v110
	v_add_u32_e32 v113, 16, v110
	v_add_u32_e32 v114, 24, v110
	v_lshl_add_u64 v[82:83], s[0:1], 0, v[152:153]
	v_mov_b32_e32 v69, v96
	v_mov_b32_e32 v85, v84
	v_mov_b32_e32 v87, v86
	v_mov_b32_e32 v89, v88
	v_mov_b32_e32 v91, v90
	v_mov_b32_e32 v93, v92
	v_mov_b32_e32 v95, v94
	v_mov_b32_e32 v97, v100
	v_lshlrev_b32_e32 v152, 2, v98
	v_add_u32_e32 v98, v2, v3
	v_add_u32_e32 v99, v4, v5
	v_readlane_b32 s5, v248, 15
	s_branch .LBB0_331

; #define LAS __attribute__((address_space(3)))
; __device__ __forceinline__ void transpose_item_fp8(const float* W, int K, int N, unsigned char* WT, float q, LAS float* scr, int item, int lane) {
;     const int nblk = N / 32, kb = item / nblk, nb = item % nblk, k0 = 64 * kb, n0 = 32 * nb;
; #pragma unroll 8
;     for (int i = 0; i < 32; ++i) { const int kk = 2 * i + (lane >> 5); scr[kk * 33 + (lane & 31)] = W[(size_t)(k0 + kk) * N + n0 + (lane & 31)]; }
.LBB0_361:
	s_lshl_b32 s11, s1, 1
	s_lshl_b32 s12, s0, 1
	v_add_u32_e32 v18, s11, v2
	v_add_u32_e32 v20, s12, v3
	v_mad_i64_i32 v[18:19], s[14:15], v18, s82, v[0:1]
	v_mad_i64_i32 v[20:21], s[14:15], v20, s82, v[0:1]
	global_load_dword v24, v[18:19], off
	global_load_dword v25, v[20:21], off
	v_add_u32_e32 v23, s11, v96
	v_add_u32_e32 v22, s12, v69
	v_mad_u64_u32 v[18:19], s[14:15], v23, s83, v[68:69]
	v_mad_u64_u32 v[20:21], s[14:15], v22, s83, v[68:69]
	v_add_u32_e32 v23, s11, v84
	v_add_u32_e32 v22, s12, v85
	s_add_i32 s1, s1, 16
	s_add_i32 s0, s0, 16
	s_add_i32 s9, s9, -16
	s_cmp_lg_u32 s9, 0
	s_waitcnt vmcnt(0)
	ds_write_b32 v18, v24
	s_waitcnt vmcnt(0)
	ds_write_b32 v20, v25
	v_add_u32_e32 v18, s11, v4
	v_add_u32_e32 v20, s12, v5
	v_mad_i64_i32 v[18:19], s[14:15], v18, s82, v[0:1]
	v_mad_i64_i32 v[20:21], s[14:15], v20, s82, v[0:1]
	global_load_dword v24, v[18:19], off
	global_load_dword v25, v[20:21], off
	v_mad_u64_u32 v[18:19], s[14:15], v23, s83, v[68:69]
	v_mad_u64_u32 v[20:21], s[14:15], v22, s83, v[68:69]
	v_add_u32_e32 v23, s11, v86
	v_add_u32_e32 v22, s12, v87
	s_waitcnt vmcnt(0)
	ds_write_b32 v18, v24
	s_waitcnt vmcnt(0)
	ds_write_b32 v20, v25
	v_add_u32_e32 v18, s11, v6
	v_add_u32_e32 v20, s12, v7
	v_mad_i64_i32 v[18:19], s[14:15], v18, s82, v[0:1]
	v_mad_i64_i32 v[20:21], s[14:15], v20, s82, v[0:1]
	global_load_dword v24, v[18:19], off
	global_load_dword v25, v[20:21], off
	v_mad_u64_u32 v[18:19], s[14:15], v23, s83, v[68:69]
	v_mad_u64_u32 v[20:21], s[14:15], v22, s83, v[68:69]
	v_add_u32_e32 v23, s11, v88
	v_add_u32_e32 v22, s12, v89
	s_waitcnt vmcnt(0)
	ds_write_b32 v18, v24
	s_waitcnt vmcnt(0)
	ds_write_b32 v20, v25
	v_add_u32_e32 v18, s11, v8
	v_add_u32_e32 v20, s12, v9
	v_mad_i64_i32 v[18:19], s[14:15], v18, s82, v[0:1]
	v_mad_i64_i32 v[20:21], s[14:15], v20, s82, v[0:1]
	global_load_dword v24, v[18:19], off
	global_load_dword v25, v[20:21], off
	v_mad_u64_u32 v[18:19], s[14:15], v23, s83, v[68:69]
	v_mad_u64_u32 v[20:21], s[14:15], v22, s83, v[68:69]
	v_add_u32_e32 v23, s11, v90
	v_add_u32_e32 v22, s12, v91
	s_waitcnt vmcnt(0)
	ds_write_b32 v18, v24
	s_waitcnt vmcnt(0)
	ds_write_b32 v20, v25
	v_add_u32_e32 v18, s11, v10
	v_add_u32_e32 v20, s12, v11
	v_mad_i64_i32 v[18:19], s[14:15], v18, s82, v[0:1]
	v_mad_i64_i32 v[20:21], s[14:15], v20, s82, v[0:1]
	global_load_dword v24, v[18:19], off
	global_load_dword v25, v[20:21], off
	v_mad_u64_u32 v[18:19], s[14:15], v23, s83, v[68:69]
	v_mad_u64_u32 v[20:21], s[14:15], v22, s83, v[68:69]
	v_add_u32_e32 v23, s11, v92
	v_add_u32_e32 v22, s12, v93
	s_waitcnt vmcnt(0)
	ds_write_b32 v18, v24
	s_waitcnt vmcnt(0)
	ds_write_b32 v20, v25
	v_add_u32_e32 v18, s11, v12
	v_add_u32_e32 v20, s12, v13
	v_mad_i64_i32 v[18:19], s[14:15], v18, s82, v[0:1]
	v_mad_i64_i32 v[20:21], s[14:15], v20, s82, v[0:1]
	global_load_dword v24, v[18:19], off
	global_load_dword v25, v[20:21], off
	v_mad_u64_u32 v[18:19], s[14:15], v23, s83, v[68:69]
	v_mad_u64_u32 v[20:21], s[14:15], v22, s83, v[68:69]
	v_add_u32_e32 v23, s11, v94
	v_add_u32_e32 v22, s12, v95
	s_waitcnt vmcnt(0)
	ds_write_b32 v18, v24
	s_waitcnt vmcnt(0)
	ds_write_b32 v20, v25
	v_add_u32_e32 v18, s11, v14
	v_add_u32_e32 v20, s12, v15
	v_mad_i64_i32 v[18:19], s[14:15], v18, s82, v[0:1]
	v_mad_i64_i32 v[20:21], s[14:15], v20, s82, v[0:1]
	global_load_dword v24, v[18:19], off
	global_load_dword v25, v[20:21], off
	v_mad_u64_u32 v[18:19], s[14:15], v23, s83, v[68:69]
	v_mad_u64_u32 v[20:21], s[14:15], v22, s83, v[68:69]
	v_add_u32_e32 v22, s12, v97
	v_add_u32_e32 v23, s11, v100
	s_waitcnt vmcnt(0)
	ds_write_b32 v18, v24
	s_waitcnt vmcnt(0)
	ds_write_b32 v20, v25
	v_add_u32_e32 v18, s11, v16
	v_add_u32_e32 v20, s12, v17
	v_mad_i64_i32 v[18:19], s[12:13], v18, s82, v[0:1]
	v_mad_i64_i32 v[20:21], s[12:13], v20, s82, v[0:1]
	global_load_dword v24, v[18:19], off
	global_load_dword v25, v[20:21], off
	v_mad_u64_u32 v[18:19], s[12:13], v23, s83, v[68:69]
	v_mad_u64_u32 v[20:21], s[12:13], v22, s83, v[68:69]
	s_waitcnt vmcnt(0)
	ds_write_b32 v18, v24
	s_waitcnt vmcnt(0)
	ds_write_b32 v20, v25
	s_cbranch_scc1 .LBB0_361
; #define LAS __attribute__((address_space(3)))
; __device__ __forceinline__ unsigned pk4_fp8(float x0, float x1, float x2, float x3) { int w = 0; w = __builtin_amdgcn_cvt_pk_fp8_f32(x0, x1, w, false); w = __builtin_amdgcn_cvt_pk_fp8_f32(x2, x3, w, true); return (unsigned)w; }
; __device__ __forceinline__ void transpose_item_fp8(const float* W, int K, int N, unsigned char* WT, float q, LAS float* scr, int item, int lane) {
;     ...
;     asm volatile("s_waitcnt lgkmcnt(0)" ::: "memory");
;     const int c = lane & 7;
; #pragma unroll
;     for (int j = 0; j < 4; ++j) { const int n = (lane >> 3) + 8 * j; const LAS float* s = scr + (8 * c) * 33 + n;
;         u32x2 o; o.x = pk4_fp8(s[0 * 33] * q, s[1 * 33] * q, s[2 * 33] * q, s[3 * 33] * q); o.y = pk4_fp8(s[4 * 33] * q, s[5 * 33] * q, s[6 * 33] * q, s[7 * 33] * q);
;         *(u32x2*)(WT + (size_t)(n0 + n) * K + k0 + 8 * c) = o; }
;     asm volatile("s_waitcnt lgkmcnt(0)" ::: "memory");
; __global__ void __launch_bounds__(512, 2) mega(Args a) {
;     ...
;             __syncthreads();
;             if (l + 1 < NLAYER && vcu >= 8) {
;                 LAS float* scr = (LAS float*)(lds + wave * 16384);
;                 for (int it = (vcu - 8) * 8 + wave; it < IT_LAYER / 2; it += (G - 8) * 8) CONVERT_ITEM(l + 1, it);
;             }
;             __syncthreads();
	s_waitcnt lgkmcnt(0)
	ds_read2_b32 v[2:3], v111 offset1:8
	ds_read2_b32 v[4:5], v111 offset0:33 offset1:41
	ds_read2_b32 v[12:13], v111 offset0:132 offset1:140
	ds_read2_b32 v[14:15], v111 offset0:165 offset1:173
	ds_read2_b32 v[6:7], v111 offset0:66 offset1:74
	ds_read2_b32 v[8:9], v111 offset0:99 offset1:107
	s_waitcnt lgkmcnt(5)
	v_mul_f32_e32 v2, 0x43000000, v2
	s_waitcnt lgkmcnt(4)
	v_mul_f32_e32 v4, 0x43000000, v4
	v_mov_b32_e32 v10, v153
	ds_read2_b32 v[16:17], v111 offset0:198 offset1:206
	ds_read2_b32 v[18:19], v111 offset0:231 offset1:239
	v_cvt_pk_fp8_f32 v10, v2, v4
	s_waitcnt lgkmcnt(5)
	v_mul_f32_e32 v2, 0x43000000, v12
	s_waitcnt lgkmcnt(4)
	v_mul_f32_e32 v4, 0x43000000, v14
	v_mov_b32_e32 v11, v153
	v_cvt_pk_fp8_f32 v11, v2, v4
	v_mul_f32_e32 v3, 0x43000000, v3
	v_mul_f32_e32 v4, 0x43000000, v5
	v_mov_b32_e32 v2, v153
	v_cvt_pk_fp8_f32 v2, v3, v4
	s_waitcnt lgkmcnt(3)
	v_mul_f32_e32 v6, 0x43000000, v6
	s_waitcnt lgkmcnt(2)
	v_mul_f32_e32 v8, 0x43000000, v8
	v_cvt_pk_fp8_f32 v10, v6, v8 op_sel:[0,0,1]
	s_waitcnt lgkmcnt(1)
	v_mul_f32_e32 v6, 0x43000000, v16
	s_waitcnt lgkmcnt(0)
	v_mul_f32_e32 v8, 0x43000000, v18
	v_cvt_pk_fp8_f32 v11, v6, v8 op_sel:[0,0,1]
	v_mul_f32_e32 v5, 0x43000000, v7
	v_mul_f32_e32 v6, 0x43000000, v9
	v_cvt_pk_fp8_f32 v2, v5, v6 op_sel:[0,0,1]
	v_mul_f32_e32 v4, 0x43000000, v13
	v_mul_f32_e32 v5, 0x43000000, v15
	v_mov_b32_e32 v3, v153
	v_cvt_pk_fp8_f32 v3, v4, v5
	v_mul_f32_e32 v6, 0x43000000, v17
	v_mul_f32_e32 v7, 0x43000000, v19
	v_add_u32_e32 v4, s8, v112
	v_cvt_pk_fp8_f32 v3, v6, v7 op_sel:[0,0,1]
	s_ashr_i32 s11, s10, 31
	v_ashrrev_i32_e32 v5, 31, v4
	v_lshl_add_u64 v[0:1], v[82:83], 0, s[10:11]
	v_lshlrev_b64 v[4:5], 10, v[4:5]
	v_lshl_add_u64 v[4:5], v[0:1], 0, v[4:5]
	global_store_dwordx2 v[4:5], v[2:3], off
	ds_read2_b32 v[2:3], v111 offset0:16 offset1:24
	ds_read2_b32 v[4:5], v111 offset0:49 offset1:57
	v_add_u32_e32 v20, s8, v110
	ds_read2_b32 v[12:13], v111 offset0:148 offset1:156
	ds_read2_b32 v[14:15], v111 offset0:181 offset1:189
	v_ashrrev_i32_e32 v21, 31, v20
	v_lshlrev_b64 v[20:21], 10, v[20:21]
	v_lshl_add_u64 v[20:21], v[0:1], 0, v[20:21]
	ds_read2_b32 v[6:7], v111 offset0:82 offset1:90
	ds_read2_b32 v[8:9], v111 offset0:115 offset1:123
	global_store_dwordx2 v[20:21], v[10:11], off
	s_waitcnt lgkmcnt(5)
	v_mul_f32_e32 v2, 0x43000000, v2
	s_waitcnt lgkmcnt(4)
	v_mul_f32_e32 v4, 0x43000000, v4
	v_mov_b32_e32 v10, v153
	ds_read2_b32 v[16:17], v111 offset0:214 offset1:222
	ds_read2_b32 v[18:19], v111 offset0:247 offset1:255
	v_cvt_pk_fp8_f32 v10, v2, v4
	s_waitcnt lgkmcnt(5)
	v_mul_f32_e32 v2, 0x43000000, v12
	s_waitcnt lgkmcnt(4)
	v_mul_f32_e32 v4, 0x43000000, v14
	v_mov_b32_e32 v11, v153
	v_cvt_pk_fp8_f32 v11, v2, v4
	v_mul_f32_e32 v3, 0x43000000, v3
	v_mul_f32_e32 v4, 0x43000000, v5
	v_mov_b32_e32 v2, v153
	v_cvt_pk_fp8_f32 v2, v3, v4
	s_waitcnt lgkmcnt(3)
	v_mul_f32_e32 v6, 0x43000000, v6
	s_waitcnt lgkmcnt(2)
	v_mul_f32_e32 v8, 0x43000000, v8
	v_cvt_pk_fp8_f32 v10, v6, v8 op_sel:[0,0,1]
	s_waitcnt lgkmcnt(1)
	v_mul_f32_e32 v6, 0x43000000, v16
	s_waitcnt lgkmcnt(0)
	v_mul_f32_e32 v8, 0x43000000, v18
	v_cvt_pk_fp8_f32 v11, v6, v8 op_sel:[0,0,1]
	v_mul_f32_e32 v5, 0x43000000, v7
	v_mul_f32_e32 v6, 0x43000000, v9
	v_cvt_pk_fp8_f32 v2, v5, v6 op_sel:[0,0,1]
	v_mul_f32_e32 v4, 0x43000000, v13
	v_mul_f32_e32 v5, 0x43000000, v15
	v_mov_b32_e32 v3, v153
	v_cvt_pk_fp8_f32 v3, v4, v5
	v_mul_f32_e32 v6, 0x43000000, v17
	v_mul_f32_e32 v7, 0x43000000, v19
	v_add_u32_e32 v20, s8, v113
	v_cvt_pk_fp8_f32 v3, v6, v7 op_sel:[0,0,1]
	v_add_u32_e32 v4, s8, v114
	v_ashrrev_i32_e32 v21, 31, v20
	v_ashrrev_i32_e32 v5, 31, v4
	v_lshlrev_b64 v[20:21], 10, v[20:21]
	v_lshlrev_b64 v[4:5], 10, v[4:5]
	v_lshl_add_u64 v[20:21], v[0:1], 0, v[20:21]
	v_lshl_add_u64 v[0:1], v[0:1], 0, v[4:5]
	global_store_dwordx2 v[20:21], v[10:11], off
	global_store_dwordx2 v[0:1], v[2:3], off
	s_waitcnt lgkmcnt(0)
	s_branch .LBB0_330
.Lb_skipconv:
	s_waitcnt vmcnt(0)
	s_barrier
.LBB0_363:
	v_readlane_b32 s0, v255, 44
	s_nop 3
	s_cmp_eq_u32 s0, 0
	s_cbranch_scc1 .Lb_fin
	s_cmp_eq_u32 s0, 2
	s_cbranch_scc0 .Lb_clr
	s_mov_b32 s0, 1
	v_writelane_b32 v255, s0, 44
	s_waitcnt vmcnt(0) lgkmcnt(0)
	s_barrier
	s_branch .Lb_reenter
.Lb_clr:
	s_mov_b32 s0, 0
	v_writelane_b32 v255, s0, 44
	s_nop 1

; #define LAS __attribute__((address_space(3)))
; #define PH_IDS() int lane_ = lane_id(); asm volatile("" : "+v"(lane_)); const int lane = lane_; const int wave = wave_s; const int tid = wave * 64 + lane; const int gw = vcu * 8 + wave; (void)lane; (void)gw; (void)tid
; __global__ void __launch_bounds__(512, 2) mega(Args a) {
;     ...
;         for (int rep_ = 0; rep_ < REPS(3); ++rep_) if (EN(3) && IN(pb + 3)) { PH_IDS();
;             for (int rnd = 0; rnd < 3; ++rnd) {
;                 int b, h, qrow0, seq, t0;
;                 if (rnd < 2) { const int u = rnd * G + vcu; if (u >= 512) continue; const int bh = u >> 5, qb = u & 31; b = bh >> 2; h = bh & 3; qrow0 = NCTX + b * SEQ + qb * 256; seq = KEYS; t0 = qb * 256; }
;                 else { const int k = vcu - 16; if (k < 0 || k >= 16 || l == NLAYER - 1) continue; b = k >> 2; h = k & 3; qrow0 = b * CTXL; seq = CTXL; t0 = -1; }
;     ...
;             if (l + 1 < NLAYER && vcu >= 32) {
;                 LAS float* scr = (LAS float*)(lds + wave * 16384);
;                 for (int it = IT_LAYER / 2 + (vcu - 32) * 8 + wave; it < IT_LAYER; it += (G - 32) * 8) CONVERT_ITEM(l + 1, it);
.Ld_reenter:
	v_readlane_b32 s0, v254, 52
	s_cmp_lg_u32 s0, 3
	s_cselect_b64 s[68:69], -1, 0
	s_andn2_b64 vcc, exec, s[60:61]
	v_readlane_b32 s1, v254, 53
	s_cbranch_vccnz .LBB0_586
	v_readlane_b32 s0, v248, 23
	v_readlane_b32 s1, v248, 24
	v_mbcnt_lo_u32_b32 v154, -1, 0
	v_mbcnt_hi_u32_b32 v154, -1, v154
	s_and_b64 s[50:51], s[0:1], s[68:69]
	v_readlane_b32 s0, v255, 45
	s_nop 3
	s_cmp_lg_u32 s0, 0
	s_cbranch_scc1 .Ld_norm
	v_readlane_b32 s0, v246, 4
	s_nop 3
	s_bitcmp1_b32 s0, 0
	s_cbranch_scc0 .Ld_norm
	s_cmp_eq_u64 s[68:69], 0
	s_cbranch_scc1 .Ld_norm
	v_readlane_b32 s0, v248, 59
	s_nop 3
	s_cmp_eq_u32 s0, 0
	s_cbranch_scc1 .Ld_norm
	v_readlane_b32 s0, v248, 62
	s_nop 3
	s_cmp_eq_u32 s0, 0
	s_cbranch_scc1 .Ld_norm
	s_mov_b32 s0, 2
	v_writelane_b32 v255, s0, 45
	v_readlane_b32 s56, v255, 14
	v_ashrrev_i32_e32 v128, 5, v154
	v_and_b32_e32 v129, 31, v154
	s_nop 1
	s_branch .Ld_conv
.Ld_norm:
	v_readlane_b32 s0, v253, 34
	v_add_u32_e32 v160, s30, v154
	s_mov_b32 s54, 0
	v_cmp_eq_u32_e64 s[40:41], 0, v160
	v_readlane_b32 s11, v255, 17
	v_readlane_b32 s10, v255, 18
	s_mov_b32 s9, s0
	v_readlane_b32 s5, v255, 19
	s_mov_b32 s8, s20
	v_readlane_b32 s4, v246, 4
	v_writelane_b32 v255, s23, 15
	v_readlane_b32 s1, v253, 35
	s_cmp_eq_u32 s54, 2
	s_cselect_b64 s[52:53], -1, 0
	s_and_b64 vcc, exec, s[52:53]
	s_cbranch_vccz .LBB0_531

; #define LAS __attribute__((address_space(3)))
; __device__ __forceinline__ unsigned pk4_fp8(float x0, float x1, float x2, float x3) { int w = 0; w = __builtin_amdgcn_cvt_pk_fp8_f32(x0, x1, w, false); w = __builtin_amdgcn_cvt_pk_fp8_f32(x2, x3, w, true); return (unsigned)w; }
; __device__ __forceinline__ void transpose_item_fp8w(const float* W, int K, int N, unsigned char* WT, float q, LAS unsigned char* scr, int item, int lane) {
;     const int nblk = N / 128, kb = item / nblk, nb = item % nblk, k0 = 64 * kb, n0 = 128 * nb;
;     const int l5 = lane & 31, h = lane >> 5;
;     const float* src = W + (size_t)(k0 + 16 * h) * N + n0 + 4 * l5;
; #pragma unroll
;     for (int b = 0; b < 2; ++b) {
;         f32x4 x[16];
; #pragma unroll
;         for (int s_ = 0; s_ < 16; ++s_) x[s_] = *(const f32x4*)(src + (size_t)(32 * b + s_) * N);
; #pragma unroll
;         for (int i = 0; i < 4; ++i) {
;             u32x4 o;
;             o.x = pk4_fp8(x[0][i] * q, x[1][i] * q, x[2][i] * q, x[3][i] * q); o.y = pk4_fp8(x[4][i] * q, x[5][i] * q, x[6][i] * q, x[7][i] * q);
;             o.z = pk4_fp8(x[8][i] * q, x[9][i] * q, x[10][i] * q, x[11][i] * q); o.w = pk4_fp8(x[12][i] * q, x[13][i] * q, x[14][i] * q, x[15][i] * q);
;             *(LAS u32x4*)(scr + (l5 + 32 * i) * 80 + (2 * b + h) * 16) = o; }
;     }
;     asm volatile("s_waitcnt lgkmcnt(0)" ::: "memory");
; #pragma unroll
;     for (int qd = 0; qd < 8; ++qd) {
;         const int rho = 16 * qd + (lane >> 2), piece = lane & 3;
; __global__ void __launch_bounds__(512, 2) mega(Args a) {
;     ...
;             if (l + 1 < NLAYER && vcu >= 32) {
;                 LAS float* scr = (LAS float*)(lds + wave * 16384);
;                 for (int it = IT_LAYER / 2 + (vcu - 32) * 8 + wave; it < IT_LAYER; it += (G - 32) * 8) CONVERT_ITEM(l + 1, it);
;                 __syncthreads();
.LBB0_658:
	v_readlane_b32 s0, v255, 45
	s_nop 3
	s_cmp_eq_u32 s0, 1
	s_cbranch_scc1 .LBB0_698
	v_readlane_b32 s0, v248, 59
	v_readlane_b32 s1, v248, 60
	s_and_b64 s[0:1], s[68:69], s[0:1]
	s_andn2_b64 vcc, exec, s[0:1]
	s_cbranch_vccnz .LBB0_699
	v_readlane_b32 s0, v248, 62
	v_readlane_b32 s1, v248, 63
	s_andn2_b64 vcc, exec, s[0:1]
	s_cbranch_vccnz .LBB0_698
.Ld_conv:
	v_ashrrev_i32_e32 v0, 1, v154
	v_lshlrev_b32_e32 v1, 4, v154
	v_and_b32_e32 v99, -16, v0
	v_ashrrev_i32_e32 v0, 2, v154
	v_and_b32_e32 v66, 48, v1
	v_and_b32_e32 v1, 0x7c, v154
	v_ashrrev_i32_e32 v4, 7, v154
	v_add_u32_e32 v104, v1, v4
	v_add_u32_e32 v4, 16, v0
	v_lshlrev_b32_e32 v5, 2, v4
	v_and_b32_e32 v5, 0x7c, v5
	v_ashrrev_i32_e32 v4, 5, v4
	v_add_u32_e32 v105, v5, v4
	v_add_u32_e32 v4, 32, v0
	v_ashrrev_i32_e32 v4, 5, v4
	v_add_u32_e32 v106, v1, v4
	v_add_u32_e32 v4, 48, v0
	v_lshlrev_b32_e32 v5, 2, v4
	v_and_b32_e32 v5, 0x7c, v5
	v_ashrrev_i32_e32 v4, 5, v4
	v_add_u32_e32 v107, v5, v4
	v_add_u32_e32 v4, 64, v0
	v_ashrrev_i32_e32 v4, 5, v4
	v_add_u32_e32 v108, v1, v4
	v_add_u32_e32 v4, 0x50, v0
	v_lshlrev_b32_e32 v5, 2, v4
	v_and_b32_e32 v5, 0x7c, v5
	v_ashrrev_i32_e32 v4, 5, v4
	s_movk_i32 s1, 0x50
	v_add_u32_e32 v109, v5, v4
	v_add_u32_e32 v4, 0x60, v0
	v_mul_lo_u32 v103, v0, s1
	v_ashrrev_i32_e32 v4, 5, v4
	v_add_u32_e32 v0, 0x70, v0
	v_add_u32_e32 v110, v1, v4
	v_lshlrev_b32_e32 v1, 2, v0
	v_and_b32_e32 v1, 0x7c, v1
	v_ashrrev_i32_e32 v0, 5, v0
	v_add_u32_e32 v111, v1, v0
	v_lshlrev_b32_e32 v0, 3, v154
	v_ashrrev_i32_e32 v112, 3, v154
	v_and_b32_e32 v152, 56, v0
	v_lshlrev_b32_e32 v64, 2, v129
	v_readlane_b32 s0, v246, 21
	v_mul_u32_u24_e32 v4, 0x84, v152
	v_lshlrev_b32_e32 v5, 2, v112
	v_add_u32_e32 v2, s0, v99
	v_add_u32_e32 v102, s0, v66
	v_add_u32_e32 v70, s0, v64
	v_add3_u32 v113, s0, v4, v5
	v_readlane_b32 s0, v255, 0
	v_mov_b32_e32 v65, v153
	v_readlane_b32 s1, v255, 1
	v_lshlrev_b32_e32 v0, 1, v152
	v_mov_b32_e32 v1, v153
	v_lshl_add_u64 v[74:75], s[0:1], 0, v[64:65]
	v_readlane_b32 s0, v255, 2
	v_readlane_b32 s1, v255, 3
	v_readlane_b32 s2, v254, 60
	v_readlane_b32 s3, v254, 61
	v_lshl_add_u64 v[76:77], s[0:1], 0, v[0:1]
	v_readlane_b32 s0, v255, 4
	v_readlane_b32 s1, v255, 5
	v_lshl_add_u64 v[68:69], s[2:3], 0, v[64:65]
	v_readlane_b32 s2, v254, 62
	v_lshl_add_u64 v[78:79], s[0:1], 0, v[64:65]
	v_readlane_b32 s0, v255, 6
	v_readlane_b32 s1, v255, 7
	v_mul_u32_u24_e32 v3, 0x50, v129
	v_readlane_b32 s3, v254, 63
	v_lshl_add_u64 v[80:81], s[0:1], 0, v[0:1]
	v_readlane_b32 s0, v255, 8
	v_readlane_b32 s1, v255, 9
	v_add_u32_e32 v86, 4, v128
	v_add_u32_e32 v88, 8, v128
	v_lshl_add_u64 v[82:83], s[0:1], 0, v[64:65]
	v_readlane_b32 s0, v255, 12
	v_readlane_b32 s1, v255, 13
	v_add_u32_e32 v90, 12, v128
	v_add_u32_e32 v92, 16, v128
	v_add_u32_e32 v94, 20, v128
	v_add_u32_e32 v96, 24, v128
	v_add_u32_e32 v98, 28, v128
	v_mov_b32_e32 v67, v153
	v_lshl_add_u64 v[72:73], s[2:3], 0, v[0:1]
	v_add_u32_e32 v114, 8, v112
	v_add_u32_e32 v115, 16, v112
	v_add_u32_e32 v116, 24, v112
	v_lshl_add_u64 v[84:85], s[0:1], 0, v[152:153]
	v_mov_b32_e32 v65, v128
	v_mov_b32_e32 v71, v86
	v_mov_b32_e32 v87, v88
	v_mov_b32_e32 v89, v90
	v_mov_b32_e32 v91, v92
	v_mov_b32_e32 v93, v94
	v_mov_b32_e32 v95, v96
	v_mov_b32_e32 v97, v98
	v_add_u32_e32 v117, v2, v3
	v_readlane_b32 s5, v248, 61
	s_branch .LBB0_662

; #define LAS __attribute__((address_space(3)))
; __global__ void __launch_bounds__(512, 2) mega(Args a) {
;     ...
;             if (l + 1 < NLAYER && vcu >= 32) {
;                 LAS float* scr = (LAS float*)(lds + wave * 16384);
;                 for (int it = IT_LAYER / 2 + (vcu - 32) * 8 + wave; it < IT_LAYER; it += (G - 32) * 8) CONVERT_ITEM(l + 1, it);
;                 __syncthreads();
;             }
.LBB0_698:
	v_readlane_b32 s0, v255, 45
	s_nop 3
	s_cmp_eq_u32 s0, 0
	s_cbranch_scc1 .Ld_fin
	s_cmp_eq_u32 s0, 2
	s_cbranch_scc0 .Ld_clr
	s_mov_b32 s0, 1
	v_writelane_b32 v255, s0, 45
	s_waitcnt vmcnt(0) lgkmcnt(0)
	s_barrier
	s_branch .Ld_reenter
.Ld_clr:
	s_mov_b32 s0, 0
	v_writelane_b32 v255, s0, 45
	s_nop 1
